# conversion split retuned: sequential-scan phase takes items up to 0x5c00 (gemm_out slack does fewer)
# speedup vs baseline: 1.0712x; 1.0018x over previous
.LBB0_139:
	s_cmpk_lt_i32 s97, 0x374
	s_cselect_b64 s[0:1], -1, 0
	v_writelane_b32 v253, s0, 15
	s_ashr_i32 s91, s97, 31
	s_ashr_i32 s76, s95, 31
	v_writelane_b32 v253, s1, 16
	s_lshr_b32 s0, s91, 29
	s_add_i32 s0, s97, s0
	s_ashr_i32 s3, s0, 3
	s_and_b32 s0, s0, -8
	s_sub_i32 s2, s97, s0
	s_mul_i32 s0, s2, 0x6e
	s_add_i32 s1, s0, 4
	s_cmp_eq_u32 s22, 15
	s_cselect_b64 s[4:5], -1, 0
	v_writelane_b32 v253, s4, 17
	s_cmp_eq_u32 s22, 14
	v_mov_b32_e32 v35, 0
	v_writelane_b32 v253, s5, 18
	s_cselect_b64 s[4:5], -1, 0
	v_writelane_b32 v253, s4, 19
	s_cmp_eq_u32 s22, 13
	v_mov_b32_e32 v250, 1
	v_writelane_b32 v253, s5, 20
	s_cselect_b64 s[4:5], -1, 0
	v_writelane_b32 v253, s4, 21
	s_cmp_eq_u32 s22, 12
	v_mov_b32_e32 v165, 0x358637bd
	v_writelane_b32 v253, s5, 22
	s_cselect_b64 s[4:5], -1, 0
	v_writelane_b32 v253, s4, 23
	s_cmp_eq_u32 s22, 11
	v_mov_b32_e32 v164, 0x3a27c5ac
	v_writelane_b32 v253, s5, 24
	s_cselect_b64 s[4:5], -1, 0
	v_writelane_b32 v253, s4, 25
	s_cmp_eq_u32 s22, 10
	v_mov_b32_e32 v200, 0x43e00000
	v_writelane_b32 v253, s5, 26
	s_cselect_b64 s[4:5], -1, 0
	v_writelane_b32 v253, s4, 27
	s_cmp_eq_u32 s22, 9
	v_mov_b32_e32 v202, 0x1a00
	v_writelane_b32 v253, s5, 28
	s_cselect_b64 s[4:5], -1, 0
	v_writelane_b32 v253, s4, 29
	s_cmp_eq_u32 s22, 8
	v_mov_b32_e32 v166, v35
	v_writelane_b32 v253, s5, 30
	s_cselect_b64 s[4:5], -1, 0
	v_writelane_b32 v253, s4, 31
	s_cmp_eq_u32 s22, 7
	v_mov_b32_e32 v167, v35
	v_writelane_b32 v253, s5, 32
	s_cselect_b64 s[4:5], -1, 0
	v_writelane_b32 v253, s4, 33
	s_cmp_eq_u32 s22, 6
	v_bfrev_b32_e32 v251, 0.5
	v_writelane_b32 v253, s5, 34
	s_cselect_b64 s[4:5], -1, 0
	v_writelane_b32 v253, s4, 35
	s_cmp_eq_u32 s22, 5
	v_mov_b32_e32 v201, 0x40e00000
	v_writelane_b32 v253, s5, 36
	s_cselect_b64 s[4:5], -1, 0
	v_writelane_b32 v253, s4, 37
	s_cmp_eq_u32 s22, 4
	v_mov_b32_e32 v168, 4.0
	v_writelane_b32 v253, s5, 38
	s_cselect_b64 s[4:5], -1, 0
	v_writelane_b32 v253, s4, 39
	s_cmp_eq_u32 s22, 3
	s_mov_b32 s53, 0xe000
	v_writelane_b32 v253, s5, 40
	s_cselect_b64 s[4:5], -1, 0
	v_writelane_b32 v253, s4, 41
	s_cmp_eq_u32 s22, 2
	s_movk_i32 s90, 0x1a00
	v_writelane_b32 v253, s5, 42
	s_cselect_b64 s[4:5], -1, 0
	v_writelane_b32 v253, s4, 43
	s_cmp_eq_u32 s22, 1
	s_movk_i32 s93, 0x5ff
	v_writelane_b32 v253, s5, 44
	s_cselect_b64 s[4:5], -1, 0
	v_writelane_b32 v253, s4, 45
	s_cmp_eq_u32 s22, 0
	s_mov_b32 s73, 0xfc000
	v_writelane_b32 v253, s5, 46
	s_cselect_b64 s[4:5], -1, 0
	s_lshl_b32 s0, s22, 6
	s_cmpk_lt_i32 s97, 0x440
	v_writelane_b32 v253, s4, 47
	s_cselect_b64 s[10:11], -1, 0
	s_cmpk_lt_i32 s95, 0x80
	v_writelane_b32 v253, s5, 48
	s_cselect_b64 s[12:13], -1, 0
	s_cmpk_lt_i32 s97, 0x1100
	v_writelane_b32 v253, s0, 49
	s_cselect_b64 s[4:5], -1, 0
	s_lshl_b32 s6, s97, 1
	v_writelane_b32 v253, s4, 50
	s_cmp_lt_i32 s97, 64
	s_mov_b32 s33, 0xc0e00000
	v_writelane_b32 v253, s5, 51
	s_cselect_b64 s[4:5], -1, 0
	v_writelane_b32 v253, s4, 52
	s_cmp_gt_i32 s97, 63
	s_mov_b64 s[20:21], 0x80
	v_writelane_b32 v253, s5, 53
	s_cselect_b64 s[4:5], -1, 0
	v_writelane_b32 v253, s4, 54
	s_lshl_b32 s0, s97, 9
	s_nop 0
	v_writelane_b32 v253, s5, 55
	v_writelane_b32 v253, s0, 56
	s_lshl_b32 s0, s95, 9
	v_writelane_b32 v253, s0, 57
	s_not_b32 s0, s97
	s_add_i32 s0, s95, s0
	s_lshl_b32 s0, s0, 9
	v_writelane_b32 v253, s0, 58
	s_sub_i32 s0, s97, 64
	s_sub_i32 s4, s95, 64
	s_cmpk_gt_i32 s97, 0x47f
	s_cselect_b64 s[8:9], -1, 0
	v_writelane_b32 v253, s8, 59
	s_lshl_b32 s5, s0, 3
	s_lshl_b32 s52, s4, 9
	v_writelane_b32 v253, s9, 60
	v_writelane_b32 v253, s5, 61
	s_lshl_b32 s5, s4, 3
	v_writelane_b32 v253, s5, 62
	v_writelane_b32 v253, s0, 63
	s_lshl_b32 s0, s0, 9
	v_writelane_b32 v254, s0, 0
	v_writelane_b32 v254, s4, 1
	v_writelane_b32 v254, s6, 2
	s_and_b32 s6, s6, 2
	s_or_b32 s7, s6, -15
	v_writelane_b32 v254, s7, 3
	s_or_b32 s7, s6, 0x3ffffd4
	s_ashr_i32 s4, s97, 1
	v_writelane_b32 v254, s7, 4
	s_and_b32 s5, s4, 1
	s_ashr_i32 s0, s97, 4
	v_writelane_b32 v254, s6, 5
	s_lshl_b32 s6, s6, 6
	s_cmp_eq_u32 s5, 0
	s_cselect_b64 s[8:9], -1, 0
	v_writelane_b32 v254, s8, 6
	s_lshl_b32 s7, s0, 12
	s_lshl_b32 s0, s0, 8
	v_writelane_b32 v254, s9, 7
	v_writelane_b32 v254, s7, 8
	s_addk_i32 s0, 0x4000
	v_writelane_b32 v254, s0, 9
	s_lshl_b32 s0, s97, 4
	v_writelane_b32 v254, s0, 10
	s_and_b32 s0, s0, 0xc0
	s_cmp_lt_i32 s2, 0
	s_cselect_b64 s[8:9], -1, 0
	v_writelane_b32 v254, s8, 11
	s_add_i32 s7, s95, -1
	s_cmp_lt_i32 s97, 32
	v_writelane_b32 v254, s9, 12
	v_writelane_b32 v254, s7, 13
	s_cselect_b64 s[8:9], -1, 0
	v_writelane_b32 v254, s8, 14
	s_lshl_b32 s14, s95, 4
	s_cmp_lt_i32 s2, 4
	v_writelane_b32 v254, s9, 15
	v_writelane_b32 v254, s2, 16
	s_mulk_i32 s2, 0x6f
	s_cselect_b32 s1, s2, s1
	s_add_i32 s1, s1, s3
	s_mul_hi_i32 s2, s1, 0x4ec4ec4f
	v_writelane_b32 v254, s3, 17
	s_lshr_b32 s3, s2, 31
	s_ashr_i32 s2, s2, 5
	s_add_i32 s2, s2, s3
	s_lshl_b32 s7, s2, 3
	s_mul_i32 s3, s2, 0x68
	s_sub_i32 s2, 0x44, s7
	s_min_u32 s8, s2, 8
	s_sub_i32 s1, s1, s3
	v_cvt_f32_ubyte0_e32 v2, s8
	v_cvt_f32_i32_e32 v1, s1
	v_rcp_iflag_f32_e32 v3, v2
	v_writelane_b32 v254, s10, 18
	s_ashr_i32 s2, s1, 30
	s_or_b32 s9, s2, 1
	v_writelane_b32 v254, s11, 19
	v_mul_f32_e32 v3, v1, v3
	v_writelane_b32 v254, s12, 20
	v_trunc_f32_e32 v3, v3
	s_and_b64 s[2:3], s[12:13], s[10:11]
	v_writelane_b32 v254, s13, 21
	v_fma_f32 v1, -v3, v2, v1
	v_writelane_b32 v254, s2, 22
	s_mul_i32 s10, s5, 0x4400
	s_mov_b32 s13, 0xc3e00000
	v_writelane_b32 v254, s3, 23
	v_cmp_ge_f32_e64 s[2:3], |v1|, v2
	v_cvt_i32_f32_e32 v1, v3
	s_and_b64 s[2:3], s[2:3], exec
	s_cselect_b32 s2, s9, 0
	s_mov_b32 s12, 0x3b800000
	v_readfirstlane_b32 s3, v1
	s_add_i32 s2, s3, s2
	s_mul_i32 s3, s2, s8
	s_abs_i32 s8, s95
	v_cvt_f32_u32_e32 v1, s8
	s_sub_i32 s1, s1, s3
	s_sext_i32_i8 s1, s1
	s_add_i32 s7, s7, s1
	v_rcp_iflag_f32_e32 v1, v1
	s_sub_i32 s1, 0, s8
	v_mul_f32_e32 v1, 0x4f7ffffe, v1
	v_cvt_u32_f32_e32 v1, v1
	s_nop 0
	v_readfirstlane_b32 s3, v1
	s_mul_i32 s1, s1, s3
	s_mul_hi_u32 s1, s3, s1
	s_add_i32 s9, s3, s1
	s_sext_i32_i8 s1, s2
	s_bfe_i64 s[2:3], s[2:3], 0x80000
	v_writelane_b32 v254, s1, 24
	s_lshl_b64 s[2:3], s[2:3], 19
	v_writelane_b32 v254, s2, 25
	s_mul_hi_u32 s1, s9, 0x374
	s_mul_i32 s1, s1, s8
	v_writelane_b32 v254, s3, 26
	v_writelane_b32 v254, s7, 27
	s_lshl_b32 s2, s7, 8
	s_sub_i32 s1, 0x374, s1
	v_writelane_b32 v254, s2, 28
	s_bitset1_b32 s2, 7
	v_writelane_b32 v254, s2, 29
	s_sub_i32 s2, s1, s8
	s_cmp_ge_u32 s1, s8
	s_cselect_b32 s1, s2, s1
	s_sub_i32 s2, s1, s8
	s_cmp_ge_u32 s1, s8
	s_cselect_b32 s1, s2, s1
	s_cmp_ge_i32 s97, s1
	s_cselect_b64 s[2:3], -1, 0
	v_writelane_b32 v254, s2, 30
	v_mbcnt_lo_u32_b32 v1, -1, 0
	v_mbcnt_hi_u32_b32 v203, -1, v1
	v_writelane_b32 v254, s3, 31
	s_sub_i32 s2, s97, s1
	s_sub_i32 s1, s95, s1
	s_lshl_b32 s49, s1, 3
	s_mul_hi_u32 s1, s9, 0x110
	s_mul_i32 s1, s1, s8
	s_lshl_b32 s2, s2, 3
	s_sub_i32 s1, 0x110, s1
	v_writelane_b32 v254, s2, 32
	s_sub_i32 s2, s1, s8
	s_cmp_ge_u32 s1, s8
	s_cselect_b32 s1, s2, s1
	v_writelane_b32 v254, s9, 33
	s_sub_i32 s2, s1, s8
	v_writelane_b32 v254, s8, 34
	s_cmp_ge_u32 s1, s8
	s_mov_b32 s8, 0
	s_cselect_b32 s1, s2, s1
	s_mov_b32 s9, 1
	s_mov_b32 s11, s8
	v_writelane_b32 v254, s10, 35
	s_cmp_ge_i32 s97, s1
	s_mul_hi_i32 s3, s4, 0x61c000
	v_writelane_b32 v254, s11, 36
	s_cselect_b64 s[10:11], -1, 0
	v_writelane_b32 v254, s10, 37
	s_sub_i32 s2, s97, s1
	s_sub_i32 s1, s95, s1
	v_writelane_b32 v254, s11, 38
	s_lshl_b32 s2, s2, 3
	s_lshl_b32 s1, s1, 3
	v_writelane_b32 v254, s1, 39
	s_add_i32 s1, s2, 0x5c00
	v_writelane_b32 v254, s1, 40
	s_lshl_b32 s1, s95, 1
	v_writelane_b32 v254, s1, 41
	s_lshl_b32 s1, s97, 11
	v_writelane_b32 v254, s1, 42
	s_lshl_b32 s1, s95, 11
	s_mul_i32 s4, s4, 0x61c000
	v_writelane_b32 v254, s1, 43
	s_add_i32 s1, s1, 0xfffe0000
	v_writelane_b32 v254, s1, 44
	s_add_u32 s1, s4, 0x796f4000
	v_writelane_b32 v254, s1, 45
	s_addc_u32 s1, s3, 0
	v_writelane_b32 v254, s1, 46
	s_or_b32 s1, s6, 0xffffef00
	v_writelane_b32 v254, s1, 47
	s_add_u32 s1, s4, 0x796f3000
	v_writelane_b32 v254, s1, 48
	s_addc_u32 s1, s3, 0
	v_writelane_b32 v254, s1, 49
	s_or_b32 s1, s6, 64
	v_writelane_b32 v254, s1, 50
	s_add_u32 s1, s4, 0x79710c00
	v_writelane_b32 v254, s1, 51
	s_addc_u32 s1, s3, 0
	v_writelane_b32 v254, s1, 52
	v_writelane_b32 v254, s4, 53
	s_add_u32 s1, s4, 0x7970fc00
	v_writelane_b32 v254, s1, 54
	v_writelane_b32 v254, s3, 55
	s_addc_u32 s1, s3, 0
	v_writelane_b32 v254, s1, 56
	s_lshl_b32 s1, s95, 6
	v_writelane_b32 v254, s1, 57
	s_add_u32 s1, s82, 0x1000
	v_writelane_b32 v254, s1, 58
	s_addc_u32 s1, s83, 0
	v_writelane_b32 v254, s1, 59
	s_lshl_b32 s0, s0, 1
	v_writelane_b32 v254, s0, 60
	s_add_i32 s0, 0, 0x20800
	v_writelane_b32 v254, s0, 61
	s_add_i32 s0, 0, 0x20804
	v_writelane_b32 v254, s0, 62
	s_add_i32 s0, 0, 0xfc0
	v_writelane_b32 v254, s0, 63
	s_add_i32 s0, 0, 0x8c00
	v_writelane_b32 v255, s0, 0
	s_add_i32 s0, 0, 0x10100
	v_writelane_b32 v255, s0, 1
	s_add_i32 s0, 0, 0x208bc
	v_writelane_b32 v255, s0, 2
	s_add_i32 s0, 0, 0x209bc
	v_writelane_b32 v255, s0, 3
	s_add_i32 s0, 0, 0x20844
	v_writelane_b32 v255, s0, 4
	s_add_i32 s0, 0, 0x2084c
	v_writelane_b32 v255, s0, 5
	s_add_i32 s0, 0, 0x20854
	v_writelane_b32 v255, s0, 6
	s_add_i32 s0, 0, 0x2085c
	v_writelane_b32 v255, s0, 7
	s_add_i32 s0, 0, 0x20864
	v_writelane_b32 v255, s0, 8
	s_add_i32 s0, 0, 0x2086c
	v_writelane_b32 v255, s0, 9
	s_add_i32 s0, 0, 0x20874
	v_writelane_b32 v255, s0, 10
	s_add_i32 s0, 0, 0x2087c
	v_writelane_b32 v255, s0, 11
	s_add_i32 s0, 0, 0x20884
	v_writelane_b32 v255, s0, 12
	s_add_i32 s0, 0, 0x2088c
	v_writelane_b32 v255, s0, 13
	s_add_i32 s0, 0, 0x20894
	v_writelane_b32 v255, s0, 14
	s_add_i32 s0, 0, 0x2089c
	v_writelane_b32 v255, s0, 15
	s_add_i32 s0, 0, 0x208a4
	v_writelane_b32 v255, s0, 16
	s_add_i32 s0, 0, 0x208ac
	s_ashr_i32 s15, s14, 31
	v_writelane_b32 v255, s0, 17
	s_add_i32 s0, 0, 0x208b4
	v_writelane_b32 v255, s0, 18
	s_lshl_b64 s[0:1], s[14:15], 12
	v_writelane_b32 v255, s0, 19
	s_nop 1
	v_writelane_b32 v255, s1, 20
	s_lshl_b64 s[0:1], s[14:15], 11
	v_writelane_b32 v255, s0, 21
	s_nop 1
	v_writelane_b32 v255, s1, 22
	s_lshl_b64 s[0:1], s[14:15], 4
	v_writelane_b32 v255, s0, 23
	s_nop 1
	v_writelane_b32 v255, s1, 24
	s_mov_b64 s[0:1], 0x10000
	v_writelane_b32 v255, s0, 25
	s_nop 1
	v_writelane_b32 v255, s1, 26
	v_writelane_b32 v255, s95, 27
	v_writelane_b32 v255, s28, 28
	s_mov_b32 s0, s14
	s_nop 0
	v_writelane_b32 v255, s29, 29
	v_writelane_b32 v255, s91, 30
	v_writelane_b32 v255, s76, 31
	v_writelane_b32 v255, s52, 32
	v_writelane_b32 v255, s0, 33
	s_nop 1
	v_writelane_b32 v255, s1, 34
	v_writelane_b32 v255, s49, 35
	v_writelane_b32 v255, s97, 36
	s_branch .LBB0_142

.LBB0_624:
	v_readlane_b32 s0, v255, 57
	s_movk_i32 s92, 0x2000
	v_readlane_b32 s1, v255, 58
	s_or_b64 exec, exec, s[0:1]
	v_readlane_b32 s0, v255, 50
	v_readlane_b32 s1, v255, 51
	s_and_b64 s[0:1], s[0:1], exec
	s_mov_b32 s0, 0xc000
	s_cselect_b32 s30, s0, 0x5c00
	v_readlane_b32 s0, v253, 14
	v_readlane_b32 s4, v255, 52
	s_add_i32 s29, s4, s0
	s_lshl_b32 s0, s4, 14
	v_readlane_b32 s80, v255, 40
	s_add_i32 s28, s0, 0
	s_add_i32 s31, s29, 0x3c00
	v_readlane_b32 s81, v255, 41
	v_readlane_b32 s84, v255, 44
	v_readlane_b32 s85, v255, 45
	v_readlane_b32 s86, v255, 46
	v_readlane_b32 s87, v255, 47
	s_cmp_ge_i32 s31, s30
	v_readlane_b32 s82, v255, 42
	v_readlane_b32 s83, v255, 43
	s_waitcnt vmcnt(0) lgkmcnt(0)
	s_barrier
	s_cbranch_scc1 .LBB0_644
	s_mul_hi_i32 s0, s31, 0x2aaaaaab
	s_lshr_b32 s1, s0, 31
	s_ashr_i32 s0, s0, 8
	s_add_i32 s0, s0, s1
	s_mul_i32 s1, s0, 0x600
	s_sub_i32 s3, s31, s1
	s_cmpk_gt_i32 s3, 0x3ff
	s_mov_b64 s[8:9], -1
	s_cbranch_scc0 .LBB0_627
	v_readlane_b32 s4, v255, 37
	s_ashr_i32 s1, s0, 31
	v_readlane_b32 s5, v255, 38
	v_readlane_b32 s36, v252, 48
	s_lshl_b32 s2, s4, 27
	s_lshl_b64 s[4:5], s[0:1], 22
	v_readlane_b32 s40, v252, 52
	v_readlane_b32 s41, v252, 53
	s_add_u32 s1, s40, s4
	s_addc_u32 s5, s41, s5
	s_add_u32 s4, s1, s2
	s_addc_u32 s5, s5, 0
	s_lshl_b32 s1, s3, 1
	s_and_b32 s1, s1, 0x7fffffc0
	s_lshl_b32 s2, s3, 5
	v_readlane_b32 s37, v252, 49
	v_readlane_b32 s38, v252, 50
	v_readlane_b32 s39, v252, 51
	v_readlane_b32 s42, v252, 54
	v_readlane_b32 s43, v252, 55
	s_addk_i32 s1, 0xf800
	s_and_b32 s2, s2, 0x3e0
	s_mov_b64 s[8:9], 0

.LBB0_770:
	s_or_b64 exec, exec, s[0:1]
	v_readlane_b32 s0, v255, 50
	v_readlane_b32 s1, v255, 51
	s_and_b64 s[0:1], s[0:1], exec
	s_mov_b32 s0, 0xc000
	s_cselect_b32 s34, s0, 0x5c00
	v_readlane_b32 s0, v253, 61
	v_readlane_b32 s1, v255, 52
	s_add_i32 s31, s1, s0
	s_lshl_b32 s0, s1, 14
	s_add_i32 s30, s0, 0
	s_add_i32 s35, s31, 0x3c00
	s_cmp_ge_i32 s35, s34
	s_cbranch_scc1 .LBB0_789
	s_mul_hi_i32 s0, s35, 0x2aaaaaab
	s_lshr_b32 s1, s0, 31
	s_ashr_i32 s0, s0, 8
	s_add_i32 s0, s0, s1
	s_mul_i32 s1, s0, 0x600
	s_sub_i32 s5, s35, s1
	s_cmpk_gt_i32 s5, 0x3ff
	s_mov_b64 s[10:11], -1
	s_cbranch_scc0 .LBB0_773
	s_ashr_i32 s1, s0, 31
	v_readlane_b32 s6, v255, 37
	v_readlane_b32 s36, v252, 48
	s_lshl_b32 s4, s6, 27
	s_lshl_b64 s[8:9], s[0:1], 22
	v_readlane_b32 s40, v252, 52
	v_readlane_b32 s41, v252, 53
	s_add_u32 s1, s40, s8
	s_addc_u32 s9, s41, s9
	s_add_u32 s8, s1, s4
	s_addc_u32 s9, s9, 0
	s_lshl_b32 s1, s5, 1
	s_and_b32 s1, s1, 0x7fffffc0
	s_lshl_b32 s4, s5, 5
	v_readlane_b32 s7, v255, 38
	v_readlane_b32 s37, v252, 49
	v_readlane_b32 s38, v252, 50
	v_readlane_b32 s39, v252, 51
	v_readlane_b32 s42, v252, 54
	v_readlane_b32 s43, v252, 55
	s_addk_i32 s1, 0xf800
	s_and_b32 s4, s4, 0x3e0
	s_mov_b64 s[10:11], 0
